# barx
# baseline (speedup 1.0000x reference)
.LBB1_4:
	s_or_b64 exec, exec, s[10:11]
	v_lshl_or_b32 v221, s2, 4, v1
	v_lshlrev_b32_e32 v10, 7, v221
	v_and_or_b32 v0, v0, 31, v10
	v_lshrrev_b32_e32 v3, 5, v220
	v_mul_lo_u32 v160, v0, 27
	v_mov_b32_e32 v161, 0
	s_add_u32 s0, s6, 0x16000
	v_mul_u32_u24_e32 v3, 14, v3
	v_lshl_add_u64 v[0:1], v[160:161], 2, s[4:5]
	v_add_u32_e32 v160, 0x360, v160
	s_addc_u32 s1, s7, 0
	v_lshlrev_b32_e32 v4, 2, v3
	v_mov_b32_e32 v5, v161
	v_lshl_add_u64 v[8:9], v[160:161], 2, s[4:5]
	v_lshl_or_b32 v160, v220, 1, v10
	v_lshl_add_u64 v[6:7], v[0:1], 0, v[4:5]
	v_lshl_add_u64 v[10:11], v[160:161], 2, s[0:1]
	v_or_b32_e32 v160, 0x400, v160
	global_load_dwordx4 v[182:185], v[6:7], off
	global_load_dwordx4 v[178:181], v[6:7], off offset:32
	global_load_dwordx4 v[198:201], v[6:7], off offset:16
	v_lshl_add_u64 v[12:13], v[160:161], 2, s[0:1]
	global_load_dwordx2 v[14:15], v[10:11], off
	global_load_dwordx2 v[16:17], v[12:13], off
	global_load_dword v222, v[0:1], off offset:52
	v_lshl_add_u64 v[0:1], v[8:9], 0, v[4:5]
	global_load_dword v223, v[0:1], off offset:48
	global_load_dwordx4 v[186:189], v[0:1], off offset:32
	global_load_dwordx4 v[194:197], v[0:1], off offset:16
	global_load_dword v225, v[6:7], off offset:48
	global_load_dwordx4 v[190:193], v[0:1], off
	global_load_dword v224, v[8:9], off offset:52
	s_add_u32 s6, s6, 0x216000
	s_load_dwordx2 s[10:11], s[12:13], 0x0
	s_load_dword s18, s[12:13], 0x8
	s_addc_u32 s7, s7, 0
	s_add_i32 s12, 0, 0x16000
	v_add_u32_e32 v228, s12, v2
	v_lshl_add_u32 v1, v220, 3, v228
	v_mov_b32_e32 v160, v161
	s_mov_b32 s16, 0
	v_cmp_gt_u32_e64 s[0:1], 32, v220
	v_cmp_eq_u32_e64 s[2:3], 0, v220
	v_mov_b32_e32 v226, 0x7f
	v_mov_b32_e32 v227, 27
	v_mov_b32_e32 v230, 0
	v_mov_b64_e32 v[218:219], v[160:161]
	s_waitcnt vmcnt(7)
	ds_write2st64_b64 v1, v[14:15], v[16:17] offset1:1
	v_mbcnt_lo_u32_b32 v1, -1, 0
	v_mbcnt_hi_u32_b32 v229, -1, v1
	s_waitcnt lgkmcnt(0)
	s_barrier
	s_waitcnt vmcnt(0)
	v_mov_b32_e32 v163, v200
	v_mov_b32_e32 v200, v179
	v_mov_b32_e32 v179, v180
	s_branch .LBB1_7
